# baseline (speedup 1.0000x reference)
.Lattn_unit:
	s_load_dwordx4 s[4:7], s[0:1], 0x0
	s_lshr_b32 s0, s2, 2
	s_and_b32 s3, s2, 7
	s_and_b32 s0, s0, 8
	s_or_b32 s30, s0, s3
	s_lshr_b32 s18, s2, 6
	s_mov_b32 s19, 0
	s_lshl_b32 s0, s2, 5
	v_readfirstlane_b32 s16, v0
	s_and_b32 s12, s0, 0x300
	s_xor_b32 s12, s12, s91
	s_lshl_b64 s[8:9], s[18:19], 15
	s_lshl_b32 s0, s30, 11
	s_lshr_b32 s33, s16, 6
	s_or_b32 s8, s8, s0
	s_or_b32 s0, s8, s12
	s_lshl_b32 s31, s33, 5
	s_add_u32 s0, s0, s31
	s_addc_u32 s1, s9, 0
	s_lshl_b64 s[0:1], s[0:1], 7
	s_waitcnt lgkmcnt(0)
	s_add_u32 s0, s4, s0
	s_addc_u32 s1, s5, s1
	s_lshl_b64 s[10:11], s[8:9], 7
	v_bfe_u32 v190, v0, 3, 3
	s_add_u32 s10, s4, s10
	v_lshl_or_b32 v182, s33, 3, v190
	s_addc_u32 s11, s5, s11
	v_lshrrev_b32_e32 v89, 1, v182
	s_add_u32 s14, s10, 0x1000000
	v_xor_b32_e32 v4, v89, v0
	s_addc_u32 s15, s11, 0
	v_mov_b32_e32 v183, 0
	v_lshlrev_b32_e32 v4, 4, v4
	s_add_u32 s10, s10, 0x2000000
	v_lshlrev_b64 v[86:87], 7, v[182:183]
	v_and_b32_e32 v1, 7, v0
	v_and_b32_e32 v182, 0x70, v4
	v_lshrrev_b32_e32 v4, 2, v0
	s_addc_u32 s11, s11, 0
	v_lshl_add_u64 v[2:3], s[14:15], 0, v[86:87]
	v_bitop3_b32 v4, v4, v1, 4 bitop3:0x6c
	v_lshl_add_u64 v[186:187], v[2:3], 0, v[182:183]
	v_lshl_add_u64 v[2:3], s[10:11], 0, v[86:87]
	v_lshlrev_b32_e32 v182, 4, v4
	s_lshl_b32 s36, s33, 10
	s_mov_b32 s13, m0
	s_mov_b32 m0, s36
	s_nop 0
	global_load_lds_dwordx4 v[186:187], off
	s_mov_b32 m0, s13
	s_mov_b64 s[20:21], 0x2000
	v_and_b32_e32 v191, 31, v0
	v_lshl_add_u64 v[194:195], v[2:3], 0, v[182:183]
	s_add_i32 s35, s36, 0x6000
	s_mov_b32 s13, m0
	s_mov_b32 m0, s35
	s_nop 0
	global_load_lds_dwordx4 v[194:195], off
	s_mov_b32 m0, s13
	v_lshl_add_u64 v[2:3], v[186:187], 0, s[20:21]
	v_bfe_u32 v88, v0, 5, 1
	s_add_i32 s37, s36, 0x2000
	s_mov_b32 s13, m0
	s_mov_b32 m0, s37
	s_nop 0
	global_load_lds_dwordx4 v[2:3], off
	s_mov_b32 m0, s13
	v_lshlrev_b32_e32 v2, 6, v191
	v_lshl_or_b32 v192, v88, 3, v2
	v_lshlrev_b32_e32 v14, 1, v192
	global_load_dwordx4 v[154:157], v14, s[0:1]
	global_load_dwordx4 v[146:149], v14, s[0:1] offset:32
	global_load_dwordx4 v[138:141], v14, s[0:1] offset:64
	global_load_dwordx4 v[134:137], v14, s[0:1] offset:96
	v_lshrrev_b32_e32 v18, 1, v0
	s_mov_b64 s[22:23], 0x4000
	v_mov_b32_e32 v2, v183
	v_mov_b32_e32 v3, v183
	v_mov_b32_e32 v4, v183
	v_mov_b32_e32 v5, v183
	v_mov_b32_e32 v6, v183
	v_mov_b32_e32 v7, v183
	v_mov_b32_e32 v8, v183
	v_mov_b32_e32 v9, v183
	v_mov_b32_e32 v10, v183
	v_mov_b32_e32 v11, v183
	v_mov_b32_e32 v12, v183
	v_mov_b32_e32 v13, v183
	v_mov_b32_e32 v14, v183
	v_mov_b32_e32 v15, v183
	v_mov_b32_e32 v16, v183
	v_mov_b32_e32 v17, v183
	v_lshlrev_b32_e32 v38, 7, v191
	v_bitop3_b32 v18, v88, v18, 7 bitop3:0x78
	v_lshl_or_b32 v211, v18, 4, v38
	v_lshl_add_u64 v[18:19], v[186:187], 0, s[22:23]
	s_add_i32 s0, s36, 0x4000
	s_mov_b32 s1, m0
	s_mov_b32 m0, s0
	s_nop 0
	global_load_lds_dwordx4 v[18:19], off
	s_mov_b32 m0, s1
	s_waitcnt vmcnt(3) lgkmcnt(0)
	s_barrier
	ds_read_b128 v[34:37], v211
	v_bfe_u32 v39, v0, 1, 3
	v_bitop3_b32 v40, v88, v39, 2 bitop3:0x36
	v_lshl_or_b32 v210, v40, 4, v38
	v_bitop3_b32 v40, v88, v39, 4 bitop3:0x36
	v_lshl_or_b32 v209, v40, 4, v38
	v_bitop3_b32 v39, v88, v39, 6 bitop3:0x36
	v_lshl_or_b32 v208, v39, 4, v38
	v_lshlrev_b32_e32 v201, 9, v88
	s_and_b32 s0, s16, 0x3fffffc0
	s_mov_b64 s[24:25], 0x6000
	s_lshl_b32 s38, s0, 2
	s_add_i32 s34, s36, 0x8000
	s_lshl_b32 s2, s2, 16
	s_lshl_b32 s3, s3, 18
	s_waitcnt vmcnt(3) lgkmcnt(0)
	v_mfma_f32_32x32x16_f16 v[18:33], v[34:37], v[154:157], v[2:17]
	ds_read_b128 v[34:37], v211 offset:4096
	s_and_b32 s2, s2, 0x200000
	s_lshl_b64 s[16:17], s[18:19], 22
	s_or_b32 s2, s2, s3
	s_or_b32 s16, s16, s2
	s_mov_b64 s[2:3], 0x1002000
	v_and_b32_e32 v90, 63, v0
	s_waitcnt lgkmcnt(0)
	v_mfma_f32_32x32x16_f16 v[2:17], v[34:37], v[154:157], v[2:17]
	ds_read_b128 v[34:37], v210
	s_mov_b32 s13, s19
	s_movk_i32 s42, 0x2000
	s_movk_i32 s39, 0x4000
	v_lshl_or_b32 v204, v191, 2, s38
	v_lshlrev_b32_e32 v212, 4, v88
	s_mov_b32 s40, -1
	s_waitcnt vmcnt(2) lgkmcnt(0)
	v_mfma_f32_32x32x16_f16 v[18:33], v[34:37], v[146:149], v[18:33]
	ds_read_b128 v[34:37], v210 offset:4096
	s_mov_b32 s41, 0x41000000
	s_mov_b32 s26, s19
	s_waitcnt lgkmcnt(0)
	v_mfma_f32_32x32x16_f16 v[2:17], v[34:37], v[146:149], v[2:17]
	ds_read_b128 v[34:37], v209
	s_waitcnt vmcnt(1) lgkmcnt(0)
	v_mfma_f32_32x32x16_f16 v[18:33], v[34:37], v[138:141], v[18:33]
	ds_read_b128 v[34:37], v209 offset:4096
	ds_read_b128 v[38:41], v208 offset:4096
	ds_read_b128 v[42:45], v208
	s_waitcnt lgkmcnt(2)
	v_mfma_f32_32x32x16_f16 v[2:17], v[34:37], v[138:141], v[2:17]
	v_lshlrev_b32_e32 v34, 5, v0
	v_lshlrev_b32_e32 v35, 1, v0
	v_lshlrev_b32_e32 v36, 3, v0
	v_and_b32_e32 v34, 0x180, v34
	v_and_b32_e32 v193, 24, v36
	v_and_or_b32 v34, v35, 32, v34
	v_or3_b32 v203, v34, v193, v201
	s_waitcnt vmcnt(0) lgkmcnt(0)
	v_mfma_f32_32x32x16_f16 v[18:33], v[42:45], v[134:137], v[18:33]
	v_and_b32_e32 v200, 64, v36
	v_bitop3_b32 v202, v36, 64, v36 bitop3:0xc
	v_or_b32_e32 v206, v203, v200
	v_or_b32_e32 v207, v203, v202
	v_mfma_f32_32x32x16_f16 v[2:17], v[38:41], v[134:137], v[2:17]
	s_nop 15
	s_nop 7
	s_nop 0
	v_max3_f32 v34, v18, v19, v2
	v_max3_f32 v35, v20, v21, v3
	s_nop 0
	v_max3_f32 v34, v34, v4, v5
	v_max3_f32 v35, v35, v24, v25
	s_nop 0
	v_max3_f32 v34, v34, v22, v23
	v_max3_f32 v35, v35, v8, v9
	s_nop 0
	v_max3_f32 v34, v34, v6, v7
	v_max3_f32 v35, v35, v28, v29
	s_nop 0
	v_max3_f32 v34, v34, v26, v27
	v_max3_f32 v35, v35, v12, v13
	s_nop 0
	v_max3_f32 v34, v34, v10, v11
	v_max3_f32 v35, v35, v32, v33
	s_nop 0
	v_max3_f32 v34, v34, v30, v31
	v_max3_f32 v35, v35, v16, v17
	s_nop 0
	v_max3_f32 v34, v34, v14, v15
	s_nop 0
	v_max_f32_e32 v34, v34, v35
	s_nop 0
	v_mov_b32_e32 v35, v34
	s_nop 1
	v_permlane32_swap_b32_e32 v34, v35
	v_max_f32_e32 v34, v34, v35
	s_nop 0
	v_add_f32_e32 v205, v183, v34
	v_sub_f32_e32 v18, v18, v34
	v_sub_f32_e32 v2, v2, v34
	v_sub_f32_e32 v19, v19, v34
	v_sub_f32_e32 v3, v3, v34
	v_sub_f32_e32 v20, v20, v34
	v_sub_f32_e32 v4, v4, v34
	v_sub_f32_e32 v21, v21, v34
	v_sub_f32_e32 v5, v5, v34
	v_sub_f32_e32 v22, v22, v34
	v_sub_f32_e32 v6, v6, v34
	v_sub_f32_e32 v23, v23, v34
	v_sub_f32_e32 v7, v7, v34
	v_sub_f32_e32 v24, v24, v34
	v_sub_f32_e32 v8, v8, v34
	v_sub_f32_e32 v25, v25, v34
	v_sub_f32_e32 v9, v9, v34
	v_sub_f32_e32 v26, v26, v34
	v_sub_f32_e32 v10, v10, v34
	v_sub_f32_e32 v27, v27, v34
	v_sub_f32_e32 v11, v11, v34
	v_sub_f32_e32 v28, v28, v34
	v_sub_f32_e32 v12, v12, v34
	v_sub_f32_e32 v29, v29, v34
	v_sub_f32_e32 v13, v13, v34
	v_sub_f32_e32 v30, v30, v34
	v_sub_f32_e32 v14, v14, v34
	v_sub_f32_e32 v31, v31, v34
	v_sub_f32_e32 v15, v15, v34
	v_sub_f32_e32 v32, v32, v34
	v_sub_f32_e32 v16, v16, v34
	v_sub_f32_e32 v33, v33, v34
	v_sub_f32_e32 v17, v17, v34
	s_nop 0
	v_xor_b32_e32 v34, 0x80000000, v205
	v_mov_b32_e32 v35, v34
	v_mov_b32_e32 v36, v34
	v_mov_b32_e32 v37, v34
	v_mov_b32_e32 v38, v34
	v_mov_b32_e32 v39, v34
	v_mov_b32_e32 v40, v34
	v_mov_b32_e32 v41, v34
	v_mov_b32_e32 v42, v34
	v_mov_b32_e32 v43, v34
	v_mov_b32_e32 v44, v34
	v_mov_b32_e32 v45, v34
	v_mov_b32_e32 v46, v34
	v_mov_b32_e32 v47, v34
	v_mov_b32_e32 v48, v34
	v_mov_b32_e32 v49, v34
	s_waitcnt vmcnt(0) lgkmcnt(0)
	s_barrier
	v_exp_f32_e32 v50, v2
	v_exp_f32_e32 v51, v3
	v_lshl_add_u64 v[2:3], v[186:187], 0, s[24:25]
	s_mov_b32 s0, m0
	s_mov_b32 m0, s36
	s_nop 0
	global_load_lds_dwordx4 v[2:3], off
	s_mov_b32 m0, s0
	v_lshl_add_u64 v[2:3], v[194:195], 0, s[20:21]
	s_mov_b32 s0, m0
	s_mov_b32 m0, s34
	s_nop 0
	global_load_lds_dwordx4 v[2:3], off
	s_mov_b32 m0, s0
	ds_read_b128 v[82:85], v211 offset:8192
	ds_read_b128 v[170:173], v211 offset:12288
	ds_read_b128 v[166:169], v210 offset:8192
	ds_read_b128 v[162:165], v210 offset:12288
	ds_read_b128 v[126:129], v209 offset:8192
	ds_read_b128 v[122:125], v209 offset:12288
	ds_read_b128 v[118:121], v208 offset:8192
	ds_read_b128 v[114:117], v208 offset:12288
	v_exp_f32_e32 v52, v4
	v_lshl_add_u64 v[2:3], s[16:17], 0, v[86:87]
	v_bitop3_b32 v4, v89, 7, v0 bitop3:0x48
	v_exp_f32_e32 v66, v18
	v_exp_f32_e32 v67, v19
	v_exp_f32_e32 v68, v20
	v_exp_f32_e32 v69, v21
	v_exp_f32_e32 v70, v22
	v_exp_f32_e32 v71, v23
	v_exp_f32_e32 v72, v24
	v_exp_f32_e32 v73, v25
	v_exp_f32_e32 v74, v26
	v_exp_f32_e32 v75, v27
	v_exp_f32_e32 v76, v28
	v_exp_f32_e32 v77, v29
	v_exp_f32_e32 v78, v30
	v_exp_f32_e32 v79, v31
	v_exp_f32_e32 v80, v32
	v_exp_f32_e32 v81, v33
	v_exp_f32_e32 v53, v5
	v_exp_f32_e32 v54, v6
	v_exp_f32_e32 v55, v7
	v_exp_f32_e32 v56, v8
	v_exp_f32_e32 v57, v9
	v_exp_f32_e32 v58, v10
	v_exp_f32_e32 v59, v11
	v_exp_f32_e32 v60, v12
	v_exp_f32_e32 v61, v13
	v_exp_f32_e32 v62, v14
	v_exp_f32_e32 v63, v15
	v_exp_f32_e32 v64, v16
	v_exp_f32_e32 v65, v17
	v_lshl_or_b32 v4, v4, 4, v2
	v_mov_b32_e32 v5, v3
	s_waitcnt vmcnt(2) lgkmcnt(0)
	s_barrier
	v_lshl_add_u64 v[4:5], s[4:5], 0, v[4:5]
	v_or_b32_e32 v2, v2, v182
	v_lshl_add_u64 v[188:189], v[4:5], 0, s[2:3]
	v_lshl_add_u64 v[2:3], s[4:5], 0, v[2:3]
	s_mov_b64 s[2:3], 0x2002000
	v_cmp_gt_u32_e64 s[0:1], 32, v90
	v_lshl_add_u64 v[196:197], v[2:3], 0, s[2:3]
	s_mov_b64 s[2:3], 0x8000
	v_mov_b32_e32 v2, v183
	v_mov_b32_e32 v3, v183
	v_mov_b32_e32 v4, v183
	v_mov_b32_e32 v5, v183
	v_mov_b32_e32 v6, v183
	v_mov_b32_e32 v7, v183
	v_mov_b32_e32 v8, v183
	v_mov_b32_e32 v9, v183
	v_mov_b32_e32 v10, v183
	v_mov_b32_e32 v11, v183
	v_mov_b32_e32 v12, v183
	v_mov_b32_e32 v13, v183
	v_mov_b32_e32 v14, v183
	v_mov_b32_e32 v15, v183
	v_mov_b32_e32 v16, v183
	v_mov_b32_e32 v17, v183
	v_mov_b32_e32 v18, v183
	v_mov_b32_e32 v19, v183
	v_mov_b32_e32 v20, v183
	v_mov_b32_e32 v21, v183
	v_mov_b32_e32 v22, v183
	v_mov_b32_e32 v23, v183
	v_mov_b32_e32 v24, v183
	v_mov_b32_e32 v25, v183
	v_mov_b32_e32 v26, v183
	v_mov_b32_e32 v27, v183
	v_mov_b32_e32 v28, v183
	v_mov_b32_e32 v29, v183
	v_mov_b32_e32 v30, v183
	v_mov_b32_e32 v31, v183
	v_mov_b32_e32 v32, v183
	v_mov_b32_e32 v33, v183
	v_subrev_u32_e32 v221, s14, v186
	v_subrev_u32_e32 v222, s10, v194
	s_add_u32 s50, s14, 0x8000
	s_addc_u32 s51, s15, 0
	s_add_u32 s52, s10, 0x4000
	s_addc_u32 s53, s11, 0
	.p2align	6

.Lu0_7:
	s_add_u32 s50, s50, 0x4000
	s_addc_u32 s51, s51, 0
	s_add_u32 s52, s52, 0x4000
	s_addc_u32 s53, s53, 0
	s_add_i32 s26, s43, 0x2000
	s_cmpk_lg_i32 s43, 0x4000
	s_cselect_b32 s27, s26, 0
	s_add_i32 s40, s40, 2
	s_cmp_lt_u32 s40, 25
	s_cbranch_scc0 .LBB2_15
	s_mov_b32 s26, s39
	s_mov_b32 s42, s43
	s_mov_b32 s39, s27
	s_branch .Lu1_1
	.p2align	6

_ZN2g34gemmILi4ELi1EEEvPKDF16_S2_PvPKfiiff:
	v_lshrrev_b32_e32 v1, 2, v0
	v_and_b32_e32 v1, 12, v1
	s_movk_i32 s18, 0x1320
	v_lshrrev_b32_e64 v1, v1, s18
	v_readfirstlane_b32 s16, v0
	v_xor_b32_e32 v1, v1, v0
	s_load_dword s12, s[0:1], 0x20
	s_load_dwordx8 s[4:11], s[0:1], 0x0
	s_lshr_b32 s17, s16, 6
	s_lshl_b32 s3, s2, 2
	v_lshlrev_b32_e32 v1, 4, v1
	v_lshlrev_b32_e32 v2, 4, v0
	s_and_b32 s14, s3, 28
	s_bfe_u32 s2, s2, 0x20003
	v_and_b32_e32 v1, 48, v1
	s_lshl_b32 s23, s17, 11
	v_and_b32_e32 v2, 0x3c0, v2
	s_or_b32 s24, s14, s2
	v_or3_b32 v100, s23, v2, v1
	v_lshrrev_b32_e32 v2, 1, v0
	s_lshr_b32 s2, s16, 2
	v_and_b32_e32 v2, 24, v2
	v_bfe_u32 v3, v0, 2, 2
	s_and_b32 s2, s2, 0x60
	s_waitcnt lgkmcnt(0)
	s_ashr_i32 s13, s12, 31
	s_lshr_b32 s14, s16, 4
	v_or3_b32 v2, v3, v2, s2
	s_and_b32 s2, s3, 0xffffff80
	s_lshl_b32 s3, s24, 14
	s_add_u32 s4, s4, s3
	s_addc_u32 s5, s5, 0
	s_ashr_i32 s3, s2, 31
	v_and_or_b32 v2, s14, 4, v2
	s_lshl_b64 s[14:15], s[2:3], 6
	s_add_u32 s6, s6, s14
	s_addc_u32 s7, s7, s15
	s_lshr_b32 s3, s16, 1
	s_and_b32 s22, s16, 64
	s_mov_b32 s16, m0
	s_mov_b32 m0, s23
	s_nop 0
	global_load_lds_dwordx4 v100, s[4:5]
	s_mov_b32 m0, s16
	v_or_b32_e32 v99, 0x400, v100
	s_lshl_b32 s25, s17, 10
	s_or_b32 s16, s23, 0x400
	s_mov_b32 s17, m0
	s_mov_b32 m0, s16
	s_nop 0
	global_load_lds_dwordx4 v99, s[4:5]
	s_mov_b32 m0, s17
	v_lshl_or_b32 v102, v2, 6, v1
	s_and_b32 s3, s3, 0x7fffffc0
	s_lshl_b64 s[14:15], s[12:13], 6
	s_add_i32 s26, s25, 0x4000
	s_mov_b32 s16, m0
	s_mov_b32 m0, s26
	s_nop 0
	global_load_lds_dwordx4 v102, s[6:7]
	s_mov_b32 m0, s16
	s_add_u32 s16, s4, 0x80000
	v_and_b32_e32 v96, 15, v0
	v_lshrrev_b32_e32 v97, 4, v0
	v_and_b32_e32 v0, 12, v0
	s_addc_u32 s17, s5, 0
	v_lshrrev_b32_e64 v0, v0, s18
	s_add_u32 s18, s6, s14
	s_addc_u32 s19, s7, s15
	s_add_i32 s20, s23, 0x6000
	s_mov_b32 s21, m0
	s_mov_b32 m0, s20
	s_nop 0
	global_load_lds_dwordx4 v100, s[16:17]
	s_mov_b32 m0, s21
	s_add_i32 s20, s23, 0x6400
	s_mov_b32 s21, m0
	s_mov_b32 m0, s20
	s_nop 0
	global_load_lds_dwordx4 v99, s[16:17]
	s_mov_b32 m0, s21
	s_add_i32 s16, s25, 0xa000
	s_mov_b32 s17, m0
	s_mov_b32 m0, s16
	s_nop 0
	global_load_lds_dwordx4 v102, s[18:19]
	s_mov_b32 m0, s17
	s_add_u32 s16, s4, 0x100000
	s_addc_u32 s17, s5, 0
	s_add_u32 s14, s18, s14
	v_xor_b32_e32 v0, v0, v97
	s_addc_u32 s15, s19, s15
	s_add_i32 s18, s23, 0xc000
	s_mov_b32 s19, m0
	s_mov_b32 m0, s18
	s_nop 0
	global_load_lds_dwordx4 v100, s[16:17]
	s_mov_b32 m0, s19
	v_lshlrev_b32_e32 v0, 4, v0
	s_add_i32 s18, s23, 0xc400
	s_mov_b32 s19, m0
	s_mov_b32 m0, s18
	s_nop 0
	global_load_lds_dwordx4 v99, s[16:17]
	s_mov_b32 m0, s19
	v_or_b32_e32 v1, s3, v96
	v_or_b32_e32 v4, s22, v96
	v_and_b32_e32 v5, 48, v0
	s_add_i32 s16, s25, 0x10000
	s_mov_b32 s17, m0
	s_mov_b32 m0, s16
	s_nop 0
	global_load_lds_dwordx4 v102, s[14:15]
	s_mov_b32 m0, s17
	v_lshl_or_b32 v98, v1, 6, v5
	s_waitcnt vmcnt(6) lgkmcnt(0)
	s_barrier
	v_lshl_or_b32 v103, v4, 6, v5
	ds_read_b128 v[28:31], v98
	ds_read_b128 v[24:27], v98 offset:1024
	ds_read_b128 v[16:19], v98 offset:2048
	ds_read_b128 v[0:3], v98 offset:3072
	ds_read_b128 v[20:23], v103 offset:16384
	ds_read_b128 v[12:15], v103 offset:17408
	ds_read_b128 v[8:11], v103 offset:18432
	ds_read_b128 v[4:7], v103 offset:19456
	s_add_u32 s14, s4, 0x180000
	v_mov_b32_e32 v84, 0
	s_movk_i32 s29, 0x6000
	v_or_b32_e32 v101, 0x4000, v103
	s_addc_u32 s15, s5, 0
	s_mul_hi_i32 s27, s12, 0xc0
	s_mul_i32 s28, s12, 0xc0
	s_lshl_b64 s[16:17], s[12:13], 7
	s_lshl_b64 s[18:19], s[12:13], 8
	s_mov_b32 s30, 0x12000
	s_mov_b32 s13, -2
	s_mov_b64 s[20:21], s[6:7]
	v_mov_b32_e32 v85, v84
	v_mov_b32_e32 v86, v84
	v_mov_b32_e32 v87, v84
	v_mov_b32_e32 v32, v84
	v_mov_b32_e32 v33, v84
	v_mov_b32_e32 v34, v84
	v_mov_b32_e32 v35, v84
	v_mov_b32_e32 v36, v84
	v_mov_b32_e32 v37, v84
	v_mov_b32_e32 v38, v84
	v_mov_b32_e32 v39, v84
	v_mov_b32_e32 v40, v84
	v_mov_b32_e32 v41, v84
	v_mov_b32_e32 v42, v84
	v_mov_b32_e32 v43, v84
	v_mov_b32_e32 v44, v84
	v_mov_b32_e32 v45, v84
	v_mov_b32_e32 v46, v84
	v_mov_b32_e32 v47, v84
	v_mov_b32_e32 v52, v84
	v_mov_b32_e32 v53, v84
	v_mov_b32_e32 v54, v84
	v_mov_b32_e32 v55, v84
	v_mov_b32_e32 v48, v84
	v_mov_b32_e32 v49, v84
	v_mov_b32_e32 v50, v84
	v_mov_b32_e32 v51, v84
	v_mov_b32_e32 v56, v84
	v_mov_b32_e32 v57, v84
	v_mov_b32_e32 v58, v84
	v_mov_b32_e32 v59, v84
	v_mov_b32_e32 v60, v84
	v_mov_b32_e32 v61, v84
	v_mov_b32_e32 v62, v84
	v_mov_b32_e32 v63, v84
	v_mov_b32_e32 v64, v84
	v_mov_b32_e32 v65, v84
	v_mov_b32_e32 v66, v84
	v_mov_b32_e32 v67, v84
	v_mov_b32_e32 v68, v84
	v_mov_b32_e32 v69, v84
	v_mov_b32_e32 v70, v84
	v_mov_b32_e32 v71, v84
	v_mov_b32_e32 v72, v84
	v_mov_b32_e32 v73, v84
	v_mov_b32_e32 v74, v84
	v_mov_b32_e32 v75, v84
	v_mov_b32_e32 v76, v84
	v_mov_b32_e32 v77, v84
	v_mov_b32_e32 v78, v84
	v_mov_b32_e32 v79, v84
	v_mov_b32_e32 v80, v84
	v_mov_b32_e32 v81, v84
	v_mov_b32_e32 v82, v84
	v_mov_b32_e32 v83, v84
	v_mov_b32_e32 v88, v84
	v_mov_b32_e32 v89, v84
	v_mov_b32_e32 v90, v84
	v_mov_b32_e32 v91, v84
	v_mov_b32_e32 v92, v84
	v_mov_b32_e32 v93, v84
	v_mov_b32_e32 v94, v84
	v_mov_b32_e32 v95, v84
	s_add_i32 s40, s23, 0x0
	s_add_i32 s41, s23, 0x400
	s_add_i32 s48, s26, 0x0
	s_add_i32 s42, s23, 0x6000
	s_add_i32 s43, s23, 0x6400
	s_add_i32 s49, s26, 0x6000
	s_add_i32 s44, s23, 0xc000
	s_add_i32 s45, s23, 0xc400
	s_add_i32 s50, s26, 0xc000
	s_add_i32 s46, s23, 0x12000
	s_add_i32 s47, s23, 0x12400
	s_add_i32 s51, s26, 0x12000
	v_add_u32_e32 v164, 0xc000, v98
	v_add_u32_e32 v165, 0xc000, v103
	.p2align	6
